# stack9: stack5 plus router logits all-reduce via DPP and permlane swaps instead of ds_bpermute, router weight reads kept four deep in flight
# speedup vs baseline: 1.0067x; 1.0067x over previous
; __device__ __forceinline__ float bflo(unsigned x) { return __uint_as_float(x << 16); }
; __device__ __forceinline__ float bfhi(unsigned x) { return __uint_as_float(x & 0xffff0000u); }
; __device__ __forceinline__ void phase_norm_route(const bf16_t* x, const float* g, const float* router, bf16_t* H, int* tok_info, unsigned* cnt, LAS unsigned char* lds, int tid, int wid, int lane) {
;     ...
;         for (int k = 0; k < 8; ++k) {
;             const int tl = wid * 8 + k, t = bt * 64 + tl;
;             u32x2 nxt[8]; { const int tn = t + (k < 7 ? 1 : 0);
; #pragma unroll
;               for (int j = 0; j < 8; ++j) nxt[j] = *(const u32x2*)(x + (size_t)tn * D + 4 * lane + 256 * j); }
;             f32x4 v[8]; { float ss = 0.f;
; #pragma unroll
;               for (int j = 0; j < 8; ++j) { const u32x2 w = raw[j]; v[j] = (f32x4){bflo(w.x), bfhi(w.x), bflo(w.y), bfhi(w.y)}; ss += (v[j][0] * v[j][0] + v[j][1] * v[j][1]) + (v[j][2] * v[j][2] + v[j][3] * v[j][3]); }
;               const float r = 1.0f / sqrtf(wave_sum(ss) * (1.0f / 2048.0f) + RMS_EPS);
.LBB0_2699:
	s_cmpk_lg_i32 s38, 0xe0
	s_cselect_b64 s[8:9], -1, 0
	v_cndmask_b32_e64 v18, 0, 1, s[8:9]
	v_mov_b32_e32 v19, s1
	v_lshl_add_u64 v[18:19], s[28:29], 0, v[18:19]
	v_lshlrev_b64 v[18:19], 12, v[18:19]
	s_waitcnt vmcnt(7) lgkmcnt(0)
	v_mov_b64_e32 v[16:17], v[108:109]
	v_lshl_add_u64 v[18:19], v[102:103], 0, v[18:19]
	s_waitcnt vmcnt(1)
	v_mov_b64_e32 v[4:5], v[122:123]
	v_mov_b64_e32 v[6:7], v[120:121]
	v_mov_b64_e32 v[8:9], v[118:119]
	v_mov_b64_e32 v[10:11], v[116:117]
	v_mov_b64_e32 v[12:13], v[114:115]
	v_mov_b64_e32 v[14:15], v[112:113]
	global_load_dwordx2 v[108:109], v[18:19], off
	global_load_dwordx2 v[112:113], v[18:19], off offset:512
	global_load_dwordx2 v[114:115], v[18:19], off offset:1024
	global_load_dwordx2 v[116:117], v[18:19], off offset:1536
	global_load_dwordx2 v[118:119], v[18:19], off offset:2048
	global_load_dwordx2 v[120:121], v[18:19], off offset:2560
	global_load_dwordx2 v[122:123], v[18:19], off offset:3072
	global_load_dwordx2 v[124:125], v[18:19], off offset:3584
	v_lshlrev_b32_e32 v18, 16, v16
	v_and_b32_e32 v19, 0xffff0000, v16
	v_lshlrev_b32_e32 v16, 16, v17
	v_and_b32_e32 v17, 0xffff0000, v17
	v_mul_f32_e32 v2, v17, v17
	v_pk_fma_f32 v[20:21], v[16:17], v[16:17], v[2:3] op_sel_hi:[1,1,0]
	v_lshlrev_b32_e32 v23, 16, v15
	v_lshlrev_b32_e32 v22, 16, v14
	v_and_b32_e32 v15, 0xffff0000, v15
	v_and_b32_e32 v14, 0xffff0000, v14
	v_mul_f32_e32 v2, v19, v19
	v_pk_mul_f32 v[24:25], v[14:15], v[14:15]
	v_lshlrev_b32_e32 v29, 16, v10
	v_pk_fma_f32 v[32:33], v[18:19], v[18:19], v[2:3] op_sel_hi:[1,1,0]
	v_pk_fma_f32 v[24:25], v[22:23], v[22:23], v[24:25]
	v_and_b32_e32 v31, 0xffff0000, v10
	v_mov_b32_e32 v28, v32
	v_mov_b32_e32 v34, v20
	v_mov_b32_e32 v35, v29
	v_and_b32_e32 v27, 0xffff0000, v12
	v_mul_f32_e32 v30, v31, v31
	v_pk_add_f32 v[20:21], v[32:33], v[20:21]
	v_pk_mul_f32 v[32:33], v[28:29], v[34:35]
	v_pk_add_f32 v[24:25], v[24:25], v[24:25] op_sel:[0,1] op_sel_hi:[1,0]
	v_lshlrev_b32_e32 v26, 16, v12
	v_lshlrev_b32_e32 v12, 16, v13
	v_and_b32_e32 v13, 0xffff0000, v13
	v_mov_b32_e32 v21, v33
	v_mov_b32_e32 v25, v30
	v_mul_f32_e32 v2, v27, v27
	v_lshlrev_b32_e32 v10, 16, v11
	v_and_b32_e32 v11, 0xffff0000, v11
	v_pk_add_f32 v[20:21], v[20:21], v[24:25]
	v_pk_fma_f32 v[24:25], v[26:27], v[26:27], v[2:3] op_sel_hi:[1,1,0]
	v_mul_f32_e32 v2, v13, v13
	v_mul_f32_e32 v68, v10, v10
	v_mul_f32_e32 v69, v11, v11
	v_pk_fma_f32 v[32:33], v[12:13], v[12:13], v[2:3] op_sel_hi:[1,1,0]
	v_mov_b32_e32 v25, v68
	v_mov_b32_e32 v33, v69
	v_pk_add_f32 v[24:25], v[24:25], v[32:33]
	v_lshlrev_b32_e32 v35, 16, v7
	v_pk_add_f32 v[20:21], v[20:21], v[24:25]
	v_lshlrev_b32_e32 v25, 16, v9
	v_lshlrev_b32_e32 v24, 16, v8
	v_and_b32_e32 v9, 0xffff0000, v9
	v_and_b32_e32 v8, 0xffff0000, v8
	v_pk_mul_f32 v[32:33], v[8:9], v[8:9]
	v_lshlrev_b32_e32 v34, 16, v6
	v_pk_fma_f32 v[32:33], v[24:25], v[24:25], v[32:33]
	v_and_b32_e32 v7, 0xffff0000, v7
	v_pk_add_f32 v[32:33], v[32:33], v[32:33] op_sel:[0,1] op_sel_hi:[1,0]
	v_and_b32_e32 v6, 0xffff0000, v6
	s_waitcnt vmcnt(8)
	v_lshlrev_b32_e32 v137, 16, v0
	v_pk_add_f32 v[20:21], v[20:21], v[20:21] op_sel:[0,1] op_sel_hi:[1,0]
	v_pk_mul_f32 v[68:69], v[6:7], v[6:7]
	v_mov_b32_e32 v136, v20
	v_mov_b32_e32 v72, v32
	v_mov_b32_e32 v73, v137
	v_pk_fma_f32 v[68:69], v[34:35], v[34:35], v[68:69]
	v_and_b32_e32 v139, 0xffff0000, v0
	v_pk_add_f32 v[20:21], v[20:21], v[32:33]
	v_pk_mul_f32 v[32:33], v[136:137], v[72:73]
	v_and_b32_e32 v71, 0xffff0000, v4
	v_mul_f32_e32 v2, v139, v139
	v_mov_b32_e32 v21, v33
	v_pk_add_f32 v[32:33], v[68:69], v[68:69] op_sel:[0,1] op_sel_hi:[1,0]
	v_lshlrev_b32_e32 v70, 16, v4
	v_lshlrev_b32_e32 v4, 16, v5
	v_and_b32_e32 v5, 0xffff0000, v5
	v_mov_b32_e32 v33, v2
	v_mul_f32_e32 v2, v71, v71
	v_lshlrev_b32_e32 v0, 16, v1
	v_and_b32_e32 v1, 0xffff0000, v1
	v_pk_add_f32 v[20:21], v[20:21], v[32:33]
	v_pk_fma_f32 v[32:33], v[70:71], v[70:71], v[2:3] op_sel_hi:[1,1,0]
	v_mul_f32_e32 v2, v5, v5
	v_mul_f32_e32 v28, v0, v0
	v_mul_f32_e32 v30, v1, v1
	v_pk_fma_f32 v[68:69], v[4:5], v[4:5], v[2:3] op_sel_hi:[1,1,0]
	v_mov_b32_e32 v33, v28
	v_mov_b32_e32 v69, v30
	v_pk_add_f32 v[32:33], v[32:33], v[68:69]
	v_mov_b32_e32 v138, v137
	v_pk_add_f32 v[20:21], v[20:21], v[32:33]
	s_nop 0
	v_add_f32_e32 v2, v20, v21
	ds_bpermute_b32 v20, v126, v2
	s_waitcnt lgkmcnt(0)
	v_add_f32_e32 v2, v2, v20
	ds_bpermute_b32 v20, v127, v2
	s_waitcnt lgkmcnt(0)
	v_add_f32_e32 v2, v2, v20
	ds_bpermute_b32 v20, v128, v2
	s_waitcnt lgkmcnt(0)
	v_add_f32_e32 v2, v2, v20
	ds_bpermute_b32 v20, v129, v2
	s_waitcnt lgkmcnt(0)
	v_add_f32_e32 v2, v2, v20
	ds_bpermute_b32 v20, v130, v2
	s_waitcnt lgkmcnt(0)
	v_add_f32_e32 v2, v2, v20
	ds_bpermute_b32 v20, v131, v2
	s_waitcnt lgkmcnt(0)
; #define LAS __attribute__((address_space(3)))
; __device__ __forceinline__ void phase_norm_route(const bf16_t* x, const float* g, const float* router, bf16_t* H, int* tok_info, unsigned* cnt, LAS unsigned char* lds, int tid, int wid, int lane) {
;     ...
;               const float r = 1.0f / sqrtf(wave_sum(ss) * (1.0f / 2048.0f) + RMS_EPS);
; #pragma unroll
;               for (int j = 0; j < 8; ++j) { v[j] = v[j] * r * gg[j]; raw[j] = nxt[j]; } }
;             { unsigned char* h8 = (unsigned char*)H + (size_t)t * D;
;               LAS unsigned char* img = lds + 69632 + wid * 9216;
; #pragma unroll
;               for (int j = 0; j < 8; ++j) *(LAS f32x4*)(img + ((lane >> 3) + 8 * j) * 144 + (lane & 7) * 16) = v[j];
;               asm volatile("s_waitcnt lgkmcnt(0)" ::: "memory");
;               pg8::v16f a, b;
; #pragma unroll
;               for (int q = 0; q < 4; ++q) { const f32x4 x = *(const LAS f32x4*)(img + lane * 144 + q * 16), y = *(const LAS f32x4*)(img + lane * 144 + 64 + q * 16);
; #pragma unroll
;                   for (int c = 0; c < 4; ++c) { a[4 * q + c] = x[c]; b[4 * q + c] = y[c]; } }
;               asm volatile("s_waitcnt lgkmcnt(0)" ::: "memory");
;               u32x4 w0, w1; pg8::mx6_block(a, b, 1.0f, w0, w1);
	v_add_f32_e32 v2, v2, v20
	v_fmamk_f32 v2, v2, 0x3a000000, v191
	v_cmp_gt_f32_e32 vcc, s39, v2
	v_mul_f32_e32 v20, 0x4f800000, v2
	s_nop 0
	v_cndmask_b32_e32 v2, v2, v20, vcc
	v_sqrt_f32_e32 v20, v2
	s_nop 0
	v_add_u32_e32 v21, -1, v20
	v_fma_f32 v28, -v21, v20, v2
	v_cmp_ge_f32_e64 s[8:9], 0, v28
	v_add_u32_e32 v28, 1, v20
	s_nop 0
	v_cndmask_b32_e64 v21, v20, v21, s[8:9]
	v_fma_f32 v20, -v28, v20, v2
	v_cmp_lt_f32_e64 s[8:9], 0, v20
	s_nop 1
	v_cndmask_b32_e64 v20, v21, v28, s[8:9]
	v_mul_f32_e32 v21, 0x37800000, v20
	v_cndmask_b32_e32 v20, v20, v21, vcc
	v_cmp_class_f32_e32 vcc, v2, v201
	s_nop 1
	v_cndmask_b32_e32 v2, v20, v2, vcc
	v_div_scale_f32 v20, s[8:9], v2, v2, 1.0
	v_rcp_f32_e32 v21, v20
	s_nop 0
	v_fma_f32 v28, -v20, v21, 1.0
	v_fmac_f32_e32 v21, v28, v21
	v_div_scale_f32 v28, vcc, 1.0, v2, 1.0
	v_mul_f32_e32 v30, v28, v21
	v_fma_f32 v32, -v20, v30, v28
	v_fmac_f32_e32 v30, v32, v21
	v_fma_f32 v20, -v20, v30, v28
	v_div_fmas_f32 v20, v20, v21, v30
	v_div_fixup_f32 v2, v20, v2, 1.0
	v_pk_mul_f32 v[10:11], v[10:11], v[2:3] op_sel_hi:[1,0]
	v_pk_mul_f32 v[16:17], v[2:3], v[16:17] op_sel_hi:[0,1]
	v_pk_mul_f32 v[86:87], v[50:51], v[10:11]
	v_mov_b32_e32 v11, v8
	v_mov_b32_e32 v8, v25
	v_pk_mul_f32 v[8:9], v[2:3], v[8:9] op_sel_hi:[0,1]
	v_pk_mul_f32 v[98:99], v[38:39], v[16:17]
	v_mov_b32_e32 v17, v14
	v_mov_b32_e32 v14, v23
	v_pk_mul_f32 v[82:83], v[54:55], v[8:9]
	v_mov_b32_e32 v9, v6
	v_mov_b32_e32 v6, v35
	v_pk_mul_f32 v[18:19], v[2:3], v[18:19] op_sel_hi:[0,1]
	v_mov_b32_e32 v16, v22
	v_pk_mul_f32 v[14:15], v[2:3], v[14:15] op_sel_hi:[0,1]
	v_pk_mul_f32 v[12:13], v[2:3], v[12:13] op_sel_hi:[0,1]
	v_mov_b32_e32 v30, v29
	v_mov_b32_e32 v10, v24
	v_mov_b32_e32 v8, v34
	v_pk_mul_f32 v[6:7], v[2:3], v[6:7] op_sel_hi:[0,1]
	v_pk_mul_f32 v[4:5], v[2:3], v[4:5] op_sel_hi:[0,1]
	v_pk_mul_f32 v[96:97], v[36:37], v[18:19]
	v_pk_mul_f32 v[16:17], v[2:3], v[16:17] op_sel_hi:[0,1]
	v_pk_mul_f32 v[94:95], v[42:43], v[14:15]
	v_pk_mul_f32 v[14:15], v[2:3], v[26:27] op_sel_hi:[0,1]
	v_pk_mul_f32 v[90:91], v[46:47], v[12:13]
	v_pk_mul_f32 v[12:13], v[30:31], v[2:3] op_sel_hi:[1,0]
	v_pk_mul_f32 v[10:11], v[2:3], v[10:11] op_sel_hi:[0,1]
	v_pk_mul_f32 v[8:9], v[2:3], v[8:9] op_sel_hi:[0,1]
	v_pk_mul_f32 v[78:79], v[58:59], v[6:7]
	v_pk_mul_f32 v[6:7], v[2:3], v[70:71] op_sel_hi:[0,1]
	v_pk_mul_f32 v[74:75], v[62:63], v[4:5]
	v_pk_mul_f32 v[4:5], v[138:139], v[2:3] op_sel_hi:[1,0]
	v_pk_mul_f32 v[0:1], v[0:1], v[2:3] op_sel_hi:[1,0]
	v_pk_mul_f32 v[92:93], v[40:41], v[16:17]
	v_pk_mul_f32 v[88:89], v[44:45], v[14:15]
	v_pk_mul_f32 v[84:85], v[48:49], v[12:13]
	v_pk_mul_f32 v[80:81], v[52:53], v[10:11]
	v_pk_mul_f32 v[76:77], v[56:57], v[8:9]
	v_pk_mul_f32 v[72:73], v[60:61], v[6:7]
	v_pk_mul_f32 v[70:71], v[66:67], v[0:1]
	v_pk_mul_f32 v[68:69], v[64:65], v[4:5]
	ds_write_b128 v101, v[96:99]
	ds_write_b128 v101, v[92:95] offset:1152
	ds_write_b128 v101, v[88:91] offset:2304
	ds_write_b128 v101, v[84:87] offset:3456
	ds_write_b128 v101, v[80:83] offset:4608
	ds_write_b128 v101, v[76:79] offset:5760
	ds_write_b128 v101, v[72:75] offset:6912
	ds_write_b128 v101, v[68:71] offset:8064
	s_waitcnt lgkmcnt(0)
	ds_read_b128 v[20:23], v135 offset:64
	ds_read_b128 v[4:7], v135
	ds_read_b128 v[8:11], v135 offset:16
	ds_read_b128 v[12:15], v135 offset:32
	ds_read_b128 v[16:19], v135 offset:48
	ds_read_b128 v[24:27], v135 offset:80
	ds_read_b128 v[28:31], v135 offset:96
	ds_read_b128 v[32:35], v135 offset:112
	s_waitcnt lgkmcnt(7)
	v_max_f32_e64 v0, |v20|, |v20|
	s_waitcnt lgkmcnt(6)
	v_max_f32_e64 v1, |v4|, |v4|
	v_max_f32_e32 v0, v1, v0
	v_max_f32_e64 v1, |v21|, |v21|
	v_max_f32_e64 v2, |v5|, |v5|
	v_max_f32_e32 v1, v2, v1
	v_max3_f32 v0, v0, 0, v1
	v_max_f32_e64 v1, |v22|, |v22|
	v_max_f32_e64 v2, |v6|, |v6|
	v_max_f32_e32 v1, v2, v1
	v_max_f32_e64 v2, |v23|, |v23|
	v_max_f32_e64 v136, |v7|, |v7|
	v_max_f32_e32 v2, v136, v2
	v_max3_f32 v0, v0, v1, v2
	s_waitcnt lgkmcnt(2)
	v_max_f32_e64 v1, |v24|, |v24|
	v_max_f32_e64 v2, |v8|, |v8|
	v_max_f32_e32 v1, v2, v1
	v_max_f32_e64 v2, |v25|, |v25|
	v_max_f32_e64 v136, |v9|, |v9|
	v_max_f32_e32 v2, v136, v2
	v_max3_f32 v0, v0, v1, v2
	v_max_f32_e64 v1, |v26|, |v26|
	v_max_f32_e64 v2, |v10|, |v10|
	v_max_f32_e32 v1, v2, v1
	v_max_f32_e64 v2, |v27|, |v27|
	v_max_f32_e64 v136, |v11|, |v11|
	v_max_f32_e32 v2, v136, v2
	v_max3_f32 v0, v0, v1, v2
	s_waitcnt lgkmcnt(1)
	v_max_f32_e64 v1, |v28|, |v28|
	v_max_f32_e64 v2, |v12|, |v12|
	v_max_f32_e32 v1, v2, v1
	v_max_f32_e64 v2, |v29|, |v29|
	v_max_f32_e64 v136, |v13|, |v13|
	v_max_f32_e32 v2, v136, v2
	v_max3_f32 v0, v0, v1, v2
	v_max_f32_e64 v1, |v30|, |v30|
	v_max_f32_e64 v2, |v14|, |v14|
	v_max_f32_e32 v1, v2, v1
	v_max_f32_e64 v2, |v31|, |v31|
	v_max_f32_e64 v136, |v15|, |v15|
	v_max_f32_e32 v2, v136, v2
	v_max3_f32 v0, v0, v1, v2
	s_waitcnt lgkmcnt(0)
	v_max_f32_e64 v1, |v32|, |v32|
	v_max_f32_e64 v2, |v16|, |v16|
	v_max_f32_e32 v1, v2, v1
	v_max_f32_e64 v2, |v33|, |v33|
	v_max_f32_e64 v136, |v17|, |v17|
	v_max_f32_e32 v2, v136, v2
	v_max3_f32 v0, v0, v1, v2
	v_max_f32_e64 v1, |v34|, |v34|
	v_max_f32_e64 v2, |v18|, |v18|
	v_max_f32_e32 v1, v2, v1
	v_max_f32_e64 v2, |v35|, |v35|
	v_max_f32_e64 v136, |v19|, |v19|
	v_max_f32_e32 v2, v136, v2
	v_max3_f32 v0, v0, v1, v2
	v_bfe_u32 v0, v0, 23, 8
	v_max_u32_e32 v0, 3, v0
	v_add_u32_e32 v2, -2, v0
	v_lshlrev_b32_e32 v0, 23, v0
	v_sub_u32_e32 v0, 0x80000000, v0
	v_pk_mul_f32 v[18:19], v[18:19], v[0:1] op_sel_hi:[1,0]
	v_pk_mul_f32 v[16:17], v[16:17], v[0:1] op_sel_hi:[1,0]
	v_pk_mul_f32 v[14:15], v[14:15], v[0:1] op_sel_hi:[1,0]
	v_pk_mul_f32 v[12:13], v[12:13], v[0:1] op_sel_hi:[1,0]
	v_pk_mul_f32 v[10:11], v[10:11], v[0:1] op_sel_hi:[1,0]
	v_pk_mul_f32 v[8:9], v[8:9], v[0:1] op_sel_hi:[1,0]
	v_pk_mul_f32 v[6:7], v[6:7], v[0:1] op_sel_hi:[1,0]
	v_pk_mul_f32 v[4:5], v[4:5], v[0:1] op_sel_hi:[1,0]
	v_pk_mul_f32 v[34:35], v[34:35], v[0:1] op_sel_hi:[1,0]
	v_pk_mul_f32 v[32:33], v[32:33], v[0:1] op_sel_hi:[1,0]
	v_pk_mul_f32 v[30:31], v[30:31], v[0:1] op_sel_hi:[1,0]
	v_pk_mul_f32 v[28:29], v[28:29], v[0:1] op_sel_hi:[1,0]
	v_pk_mul_f32 v[26:27], v[26:27], v[0:1] op_sel_hi:[1,0]
	v_pk_mul_f32 v[24:25], v[24:25], v[0:1] op_sel_hi:[1,0]
	v_pk_mul_f32 v[22:23], v[22:23], v[0:1] op_sel_hi:[1,0]
	v_pk_mul_f32 v[20:21], v[20:21], v[0:1] op_sel_hi:[1,0]
	s_waitcnt lgkmcnt(0)
; #define LAS __attribute__((address_space(3)))
; __device__ __forceinline__ void mx6_block(const v16f& a, const v16f& b, float pre, u32x4& w0, u32x4& w1) {
;     float amax = 0.f;
; #pragma unroll
;     for (int i = 0; i < 16; ++i) amax = fmaxf(amax, fmaxf(__builtin_fabsf(a[i]), __builtin_fabsf(b[i])));
;     amax *= __builtin_fabsf(pre);
;     int eb = (int)((__float_as_uint(amax) >> 23) & 0xFFu) - 2; eb = eb < 1 ? 1 : eb;
;     const float mul = pre * __uint_as_float((unsigned)(254 - eb) << 23);
;     const v16f as = a * mul, bs = b * mul;
;     const auto r = __builtin_amdgcn_cvt_scalef32_2xpk16_fp6_f32(as, bs, 1.0f);
;     w0 = (u32x4){(unsigned)r[0], (unsigned)r[1], (unsigned)r[2], (unsigned)r[3]}; w1 = (u32x4){(unsigned)r[4], (unsigned)r[5], (unsigned)eb, 0u};
; __device__ __forceinline__ void phase_norm_route(const bf16_t* x, const float* g, const float* router, bf16_t* H, int* tok_info, unsigned* cnt, LAS unsigned char* lds, int tid, int wid, int lane) {
;     ...
;               u32x4 w0, w1; pg8::mx6_block(a, b, 1.0f, w0, w1);
;               unsigned char* q = h8 + (lane >> 2) * 128 + (lane & 3) * 16;
;               *(u32x4*)q = w0; *(u32x4*)(q + 64) = w1; }
;             float lg[8];
; #pragma unroll
;             for (int e = 0; e < 8; ++e) { float s = 0.f;
; #pragma unroll
;                 for (int j = 0; j < 8; ++j) { const f32x4 r = *(const LAS f32x4*)(RT + e * 2048 + 4 * lane + 256 * j); s += (v[j][0] * r[0] + v[j][1] * r[1]) + (v[j][2] * r[2] + v[j][3] * r[3]); }
;                 lg[e] = wave_sum(s); }
	s_nop 0
	v_cvt_scalef32_2xpk16_fp6_f32 v[4:9], v[4:19], v[20:35], 1.0
	v_mov_b32_e32 v0, v8
	v_mov_b32_e32 v1, v9
	global_store_dwordx4 v[110:111], v[4:7], off
	global_store_dwordx4 v[110:111], v[0:3], off offset:64
	ds_read_b128 v[20:23], v133
	ds_read_b128 v[24:27], v133 offset:1024
	ds_read_b128 v[28:31], v133 offset:2048
	ds_read_b128 v[32:35], v133 offset:3072
	ds_read_b128 v[16:19], v133 offset:4096
	ds_read_b128 v[12:15], v133 offset:5120
	ds_read_b128 v[8:11], v133 offset:6144
	ds_read_b128 v[4:7], v133 offset:7168
	ds_read_b128 v[136:139], v133 offset:8192
	ds_read_b128 v[140:143], v133 offset:9216
	s_waitcnt lgkmcnt(9)
	v_mov_b32_e32 v1, v21
	s_waitcnt lgkmcnt(1)
	v_mov_b32_e32 v0, v136
	v_pk_mul_f32 v[0:1], v[96:97], v[0:1]
	v_pk_mov_b32 v[20:21], v[136:137], v[20:21] op_sel:[1,0]
	s_nop 0
	v_pk_fma_f32 v[0:1], v[96:97], v[20:21], v[0:1] op_sel:[1,0,0] op_sel_hi:[0,1,1]
	v_mov_b32_e32 v20, v138
	v_mov_b32_e32 v21, v23
	v_pk_mul_f32 v[20:21], v[98:99], v[20:21]
	v_pk_mov_b32 v[22:23], v[138:139], v[22:23] op_sel:[1,0]
	s_nop 0
	v_pk_fma_f32 v[20:21], v[98:99], v[22:23], v[20:21] op_sel:[1,0,0] op_sel_hi:[0,1,1]
	v_pk_add_f32 v[0:1], v[0:1], v[20:21]
	s_waitcnt lgkmcnt(0)
	v_mov_b32_e32 v20, v140
	v_mov_b32_e32 v21, v25
	v_pk_mul_f32 v[20:21], v[92:93], v[20:21]
	v_pk_mov_b32 v[22:23], v[140:141], v[24:25] op_sel:[1,0]
	v_pk_mov_b32 v[24:25], v[142:143], v[26:27] op_sel:[1,0]
	v_pk_fma_f32 v[20:21], v[92:93], v[22:23], v[20:21] op_sel:[1,0,0] op_sel_hi:[0,1,1]
	v_mov_b32_e32 v22, v142
	v_mov_b32_e32 v23, v27
	v_pk_mul_f32 v[22:23], v[94:95], v[22:23]
	v_pk_add_f32 v[0:1], v[0:1], 0 op_sel_hi:[1,0]
	v_pk_fma_f32 v[22:23], v[94:95], v[24:25], v[22:23] op_sel:[1,0,0] op_sel_hi:[0,1,1]
	v_pk_add_f32 v[20:21], v[20:21], v[22:23]
	v_mov_b32_e32 v25, v29
	v_pk_add_f32 v[0:1], v[0:1], v[20:21]
	ds_read_b128 v[20:23], v133 offset:10240
	s_waitcnt lgkmcnt(0)
	v_mov_b32_e32 v24, v20
	v_pk_mul_f32 v[24:25], v[88:89], v[24:25]
	v_pk_mov_b32 v[20:21], v[20:21], v[28:29] op_sel:[1,0]
	s_nop 0
	v_pk_fma_f32 v[20:21], v[88:89], v[20:21], v[24:25] op_sel:[1,0,0] op_sel_hi:[0,1,1]
	v_mov_b32_e32 v24, v22
	v_mov_b32_e32 v25, v31
	v_pk_mul_f32 v[24:25], v[90:91], v[24:25]
	v_pk_mov_b32 v[22:23], v[22:23], v[30:31] op_sel:[1,0]
	s_nop 0
	v_pk_fma_f32 v[22:23], v[90:91], v[22:23], v[24:25] op_sel:[1,0,0] op_sel_hi:[0,1,1]
	v_pk_add_f32 v[136:137], v[20:21], v[22:23]
	ds_read_b128 v[20:23], v133 offset:11264
	v_mov_b32_e32 v25, v33
	v_pk_add_f32 v[0:1], v[0:1], v[136:137]
	s_waitcnt lgkmcnt(0)
	v_mov_b32_e32 v24, v20
	v_pk_mul_f32 v[24:25], v[84:85], v[24:25]
	v_pk_mov_b32 v[20:21], v[20:21], v[32:33] op_sel:[1,0]
	s_nop 0
	v_pk_fma_f32 v[138:139], v[84:85], v[20:21], v[24:25] op_sel:[1,0,0] op_sel_hi:[0,1,1]
	v_mov_b32_e32 v20, v22
	v_mov_b32_e32 v21, v35
	v_pk_mul_f32 v[20:21], v[86:87], v[20:21]
	v_pk_mov_b32 v[22:23], v[22:23], v[34:35] op_sel:[1,0]
	v_mov_b32_e32 v25, v17
	v_pk_fma_f32 v[140:141], v[86:87], v[22:23], v[20:21] op_sel:[1,0,0] op_sel_hi:[0,1,1]
	ds_read_b128 v[20:23], v133 offset:12288
	v_pk_add_f32 v[136:137], v[138:139], v[140:141]
	s_waitcnt lgkmcnt(0)
	v_mov_b32_e32 v24, v20
	v_pk_mul_f32 v[142:143], v[80:81], v[24:25]
	v_mov_b32_e32 v24, v22
	v_mov_b32_e32 v25, v19
	v_pk_mul_f32 v[144:145], v[82:83], v[24:25]
	ds_read_b128 v[24:27], v133 offset:13312
	ds_read_b128 v[28:31], v133 offset:14336
	ds_read_b128 v[32:35], v133 offset:15360
	v_pk_mov_b32 v[16:17], v[20:21], v[16:17] op_sel:[1,0]
	v_pk_mov_b32 v[18:19], v[22:23], v[18:19] op_sel:[1,0]
	v_pk_fma_f32 v[16:17], v[80:81], v[16:17], v[142:143] op_sel:[1,0,0] op_sel_hi:[0,1,1]
	v_pk_fma_f32 v[18:19], v[82:83], v[18:19], v[144:145] op_sel:[1,0,0] op_sel_hi:[0,1,1]
	v_pk_add_f32 v[0:1], v[0:1], v[136:137]
	v_pk_add_f32 v[16:17], v[16:17], v[18:19]
	s_nop 0
	v_pk_add_f32 v[0:1], v[0:1], v[16:17]
	s_waitcnt lgkmcnt(2)
	v_mov_b32_e32 v16, v24
	v_mov_b32_e32 v17, v13
	v_pk_mul_f32 v[16:17], v[76:77], v[16:17]
	v_pk_mov_b32 v[12:13], v[24:25], v[12:13] op_sel:[1,0]
	s_nop 0
	v_pk_fma_f32 v[12:13], v[76:77], v[12:13], v[16:17] op_sel:[1,0,0] op_sel_hi:[0,1,1]
	v_mov_b32_e32 v16, v26
	v_mov_b32_e32 v17, v15
	v_pk_mul_f32 v[16:17], v[78:79], v[16:17]
	v_pk_mov_b32 v[14:15], v[26:27], v[14:15] op_sel:[1,0]
	s_nop 0
	v_pk_fma_f32 v[14:15], v[78:79], v[14:15], v[16:17] op_sel:[1,0,0] op_sel_hi:[0,1,1]
	v_pk_add_f32 v[12:13], v[12:13], v[14:15]
	s_nop 0
	v_pk_add_f32 v[0:1], v[0:1], v[12:13]
	s_waitcnt lgkmcnt(1)
	v_mov_b32_e32 v12, v28
	v_mov_b32_e32 v13, v9
	v_pk_mul_f32 v[12:13], v[72:73], v[12:13]
	v_pk_mov_b32 v[8:9], v[28:29], v[8:9] op_sel:[1,0]
	s_nop 0
	v_pk_fma_f32 v[8:9], v[72:73], v[8:9], v[12:13] op_sel:[1,0,0] op_sel_hi:[0,1,1]
	v_mov_b32_e32 v12, v30
	v_mov_b32_e32 v13, v11
	v_pk_mul_f32 v[12:13], v[74:75], v[12:13]
	v_pk_mov_b32 v[10:11], v[30:31], v[10:11] op_sel:[1,0]
	s_nop 0
	v_pk_fma_f32 v[10:11], v[74:75], v[10:11], v[12:13] op_sel:[1,0,0] op_sel_hi:[0,1,1]
	v_pk_add_f32 v[8:9], v[8:9], v[10:11]
	s_nop 0
	v_pk_add_f32 v[0:1], v[0:1], v[8:9]
	s_waitcnt lgkmcnt(0)
; #define LAS __attribute__((address_space(3)))
; __device__ __forceinline__ float wave_sum(float v) {
; #pragma unroll
;     for (int o = 1; o < 64; o <<= 1) v += __shfl_xor(v, o);
;     return v;
; __device__ __forceinline__ void phase_norm_route(const bf16_t* x, const float* g, const float* router, bf16_t* H, int* tok_info, unsigned* cnt, LAS unsigned char* lds, int tid, int wid, int lane) {
;     ...
;             float lg[8];
; #pragma unroll
;             for (int e = 0; e < 8; ++e) { float s = 0.f;
; #pragma unroll
;                 for (int j = 0; j < 8; ++j) { const f32x4 r = *(const LAS f32x4*)(RT + e * 2048 + 4 * lane + 256 * j); s += (v[j][0] * r[0] + v[j][1] * r[1]) + (v[j][2] * r[2] + v[j][3] * r[3]); }
;                 lg[e] = wave_sum(s); }
	v_mov_b32_e32 v8, v32
	v_mov_b32_e32 v9, v5
	v_pk_mul_f32 v[8:9], v[68:69], v[8:9]
	v_pk_mov_b32 v[4:5], v[32:33], v[4:5] op_sel:[1,0]
	s_nop 0
	v_pk_fma_f32 v[4:5], v[68:69], v[4:5], v[8:9] op_sel:[1,0,0] op_sel_hi:[0,1,1]
	v_mov_b32_e32 v8, v34
	v_mov_b32_e32 v9, v7
	v_pk_mul_f32 v[8:9], v[70:71], v[8:9]
	v_pk_mov_b32 v[6:7], v[34:35], v[6:7] op_sel:[1,0]
	s_nop 0
	v_pk_fma_f32 v[6:7], v[70:71], v[6:7], v[8:9] op_sel:[1,0,0] op_sel_hi:[0,1,1]
	v_pk_add_f32 v[4:5], v[4:5], v[6:7]
	ds_read_b128 v[208:211], v133 offset:16384
	ds_read_b128 v[212:215], v133 offset:17408
	ds_read_b128 v[216:219], v133 offset:18432
	ds_read_b128 v[220:223], v133 offset:19456
	ds_read_b128 v[224:227], v133 offset:20480
	v_pk_add_f32 v[0:1], v[0:1], v[4:5]
	s_nop 1
	v_add_f32_dpp v0, v0, v0 quad_perm:[1,0,3,2] row_mask:0xf bank_mask:0xf
	s_nop 1
	v_add_f32_dpp v0, v0, v0 quad_perm:[2,3,0,1] row_mask:0xf bank_mask:0xf
	s_nop 1
	v_add_f32_dpp v0, v0, v0 row_half_mirror row_mask:0xf bank_mask:0xf
	s_nop 1
	v_add_f32_dpp v0, v0, v0 row_mirror row_mask:0xf bank_mask:0xf
	v_mov_b32_e32 v4, v0
	s_nop 1
	v_permlane16_swap_b32_e32 v4, v0
	v_add_f32_e32 v0, v0, v4
	v_mov_b32_e32 v4, v0
	s_nop 1
	v_permlane32_swap_b32_e32 v4, v0
	v_add_f32_e32 v0, v0, v4
	s_nop 1
	v_add_f32_dpp v1, v1, v1 quad_perm:[1,0,3,2] row_mask:0xf bank_mask:0xf
	s_nop 1
	v_add_f32_dpp v1, v1, v1 quad_perm:[2,3,0,1] row_mask:0xf bank_mask:0xf
	s_nop 1
	v_add_f32_dpp v1, v1, v1 row_half_mirror row_mask:0xf bank_mask:0xf
	s_nop 1
	v_add_f32_dpp v1, v1, v1 row_mirror row_mask:0xf bank_mask:0xf
	v_mov_b32_e32 v5, v1
	s_nop 1
	v_permlane16_swap_b32_e32 v5, v1
	v_add_f32_e32 v1, v1, v5
	v_mov_b32_e32 v5, v1
	s_nop 1
	v_permlane32_swap_b32_e32 v5, v1
	v_add_f32_e32 v1, v1, v5
	s_nop 0
	s_waitcnt lgkmcnt(4)
	v_mul_f32_e32 v2, v97, v209
	v_fmac_f32_e32 v2, v96, v208
	v_mul_f32_e32 v6, v99, v211
	v_fmac_f32_e32 v6, v98, v210
	v_add_f32_e32 v2, v2, v6
	ds_read_b128 v[228:231], v133 offset:21504
	v_add_f32_e32 v2, 0, v2
	s_waitcnt lgkmcnt(5)
	s_nop 0
	s_nop 0
	s_nop 0
	s_waitcnt lgkmcnt(4)
	v_mul_f32_e32 v7, v93, v213
	v_fmac_f32_e32 v7, v92, v212
	v_mul_f32_e32 v6, v95, v215
	v_fmac_f32_e32 v6, v94, v214
	v_add_f32_e32 v6, v7, v6
	v_add_f32_e32 v2, v2, v6
	ds_read_b128 v[208:211], v133 offset:22528
	s_waitcnt lgkmcnt(5)
	s_nop 0
	s_nop 0
	s_nop 0
	s_waitcnt lgkmcnt(4)
	v_mul_f32_e32 v7, v89, v217
	v_fmac_f32_e32 v7, v88, v216
	v_mul_f32_e32 v6, v91, v219
	v_fmac_f32_e32 v6, v90, v218
	v_add_f32_e32 v6, v7, v6
	v_add_f32_e32 v2, v2, v6
	ds_read_b128 v[212:215], v133 offset:23552
	s_waitcnt lgkmcnt(5)
	s_nop 0
	s_nop 0
	s_nop 0
	s_waitcnt lgkmcnt(4)
	v_mul_f32_e32 v7, v85, v221
	v_fmac_f32_e32 v7, v84, v220
	v_mul_f32_e32 v6, v87, v223
	v_fmac_f32_e32 v6, v86, v222
	v_add_f32_e32 v6, v7, v6
	v_add_f32_e32 v2, v2, v6
	ds_read_b128 v[216:219], v133 offset:24576
	s_waitcnt lgkmcnt(5)
	s_nop 0
	s_nop 0
	s_nop 0
	s_waitcnt lgkmcnt(4)
	v_mul_f32_e32 v7, v81, v225
	v_fmac_f32_e32 v7, v80, v224
	v_mul_f32_e32 v6, v83, v227
	v_fmac_f32_e32 v6, v82, v226
	v_add_f32_e32 v6, v7, v6
	v_add_f32_e32 v2, v2, v6
	ds_read_b128 v[220:223], v133 offset:25600
	s_waitcnt lgkmcnt(5)
	s_nop 0
	s_nop 0
	s_nop 0
	s_waitcnt lgkmcnt(4)
	v_mul_f32_e32 v7, v77, v229
	v_fmac_f32_e32 v7, v76, v228
	v_mul_f32_e32 v6, v79, v231
	v_fmac_f32_e32 v6, v78, v230
	v_add_f32_e32 v6, v7, v6
	v_add_f32_e32 v2, v2, v6
	ds_read_b128 v[224:227], v133 offset:26624
	s_waitcnt lgkmcnt(4)
	v_mul_f32_e32 v7, v73, v209
	v_fmac_f32_e32 v7, v72, v208
	v_mul_f32_e32 v6, v75, v211
	v_fmac_f32_e32 v6, v74, v210
	v_add_f32_e32 v6, v7, v6
	v_add_f32_e32 v2, v2, v6
	ds_read_b128 v[228:231], v133 offset:27648
	s_waitcnt lgkmcnt(4)
	v_mul_f32_e32 v7, v69, v213
	v_fmac_f32_e32 v7, v68, v212
	v_mul_f32_e32 v6, v71, v215
	v_fmac_f32_e32 v6, v70, v214
	ds_read_b128 v[208:211], v133 offset:28672
	v_add_f32_e32 v6, v7, v6
	v_add_f32_e32 v2, v2, v6
	s_nop 1
	v_add_f32_dpp v2, v2, v2 quad_perm:[1,0,3,2] row_mask:0xf bank_mask:0xf
	s_nop 1
	v_add_f32_dpp v2, v2, v2 quad_perm:[2,3,0,1] row_mask:0xf bank_mask:0xf
	s_nop 1
	v_add_f32_dpp v2, v2, v2 row_half_mirror row_mask:0xf bank_mask:0xf
	s_nop 1
	v_add_f32_dpp v2, v2, v2 row_mirror row_mask:0xf bank_mask:0xf
	v_mov_b32_e32 v6, v2
	s_nop 1
	v_permlane16_swap_b32_e32 v6, v2
	v_add_f32_e32 v2, v2, v6
	v_mov_b32_e32 v6, v2
	s_nop 1
	v_permlane32_swap_b32_e32 v6, v2
	v_add_f32_e32 v2, v2, v6
	s_waitcnt lgkmcnt(4)
	v_mul_f32_e32 v7, v97, v217
	v_fmac_f32_e32 v7, v96, v216
	v_mul_f32_e32 v8, v99, v219
	v_fmac_f32_e32 v8, v98, v218
	v_add_f32_e32 v7, v7, v8
	ds_read_b128 v[212:215], v133 offset:29696
	v_add_f32_e32 v7, 0, v7
	s_waitcnt lgkmcnt(5)
	s_nop 0
	s_nop 0
	s_waitcnt lgkmcnt(4)
	v_mul_f32_e32 v9, v93, v221
	v_fmac_f32_e32 v9, v92, v220
	v_mul_f32_e32 v8, v95, v223
	v_fmac_f32_e32 v8, v94, v222
	v_add_f32_e32 v8, v9, v8
	v_add_f32_e32 v7, v7, v8
	ds_read_b128 v[216:219], v133 offset:30720
	s_waitcnt lgkmcnt(5)
	s_nop 0
	s_nop 0
	s_waitcnt lgkmcnt(4)
	v_mul_f32_e32 v9, v89, v225
	v_fmac_f32_e32 v9, v88, v224
	v_mul_f32_e32 v8, v91, v227
	v_fmac_f32_e32 v8, v90, v226
	v_add_f32_e32 v8, v9, v8
	v_add_f32_e32 v7, v7, v8
	ds_read_b128 v[220:223], v133 offset:31744
	s_waitcnt lgkmcnt(5)
	s_nop 0
	s_nop 0
	s_waitcnt lgkmcnt(4)
	v_mul_f32_e32 v9, v85, v229
	v_fmac_f32_e32 v9, v84, v228
	v_mul_f32_e32 v8, v87, v231
	v_fmac_f32_e32 v8, v86, v230
	v_add_f32_e32 v8, v9, v8
	v_add_f32_e32 v7, v7, v8
	ds_read_b128 v[224:227], v133 offset:32768
	s_waitcnt lgkmcnt(5)
	s_nop 0
	s_nop 0
	s_waitcnt lgkmcnt(4)
	v_mul_f32_e32 v9, v81, v209
	v_fmac_f32_e32 v9, v80, v208
	v_mul_f32_e32 v8, v83, v211
	v_fmac_f32_e32 v8, v82, v210
	v_add_f32_e32 v8, v9, v8
	v_add_f32_e32 v7, v7, v8
	ds_read_b128 v[228:231], v133 offset:33792
	s_waitcnt lgkmcnt(5)
; #define LAS __attribute__((address_space(3)))
; __device__ __forceinline__ void phase_norm_route(const bf16_t* x, const float* g, const float* router, bf16_t* H, int* tok_info, unsigned* cnt, LAS unsigned char* lds, int tid, int wid, int lane) {
;     ...
;             float lg[8];
; #pragma unroll
;             for (int e = 0; e < 8; ++e) { float s = 0.f;
; #pragma unroll
;                 for (int j = 0; j < 8; ++j) { const f32x4 r = *(const LAS f32x4*)(RT + e * 2048 + 4 * lane + 256 * j); s += (v[j][0] * r[0] + v[j][1] * r[1]) + (v[j][2] * r[2] + v[j][3] * r[3]); }
;                 lg[e] = wave_sum(s); }
	s_nop 0
	s_nop 0
	s_waitcnt lgkmcnt(4)
	v_mul_f32_e32 v9, v77, v213
	v_fmac_f32_e32 v9, v76, v212
	v_mul_f32_e32 v8, v79, v215
	v_fmac_f32_e32 v8, v78, v214
	v_add_f32_e32 v8, v9, v8
	v_add_f32_e32 v7, v7, v8
	ds_read_b128 v[208:211], v133 offset:34816
	s_waitcnt lgkmcnt(4)
	v_mul_f32_e32 v9, v73, v217
	v_fmac_f32_e32 v9, v72, v216
	v_mul_f32_e32 v8, v75, v219
	v_fmac_f32_e32 v8, v74, v218
	v_add_f32_e32 v8, v9, v8
	v_add_f32_e32 v7, v7, v8
	ds_read_b128 v[212:215], v133 offset:35840
	s_waitcnt lgkmcnt(4)
	v_mul_f32_e32 v9, v69, v221
	v_fmac_f32_e32 v9, v68, v220
	v_mul_f32_e32 v8, v71, v223
	v_fmac_f32_e32 v8, v70, v222
	ds_read_b128 v[216:219], v133 offset:36864
	v_add_f32_e32 v8, v9, v8
	v_add_f32_e32 v7, v7, v8
	s_nop 1
	v_add_f32_dpp v7, v7, v7 quad_perm:[1,0,3,2] row_mask:0xf bank_mask:0xf
	s_nop 1
	v_add_f32_dpp v7, v7, v7 quad_perm:[2,3,0,1] row_mask:0xf bank_mask:0xf
	s_nop 1
	v_add_f32_dpp v7, v7, v7 row_half_mirror row_mask:0xf bank_mask:0xf
	s_nop 1
	v_add_f32_dpp v7, v7, v7 row_mirror row_mask:0xf bank_mask:0xf
	v_mov_b32_e32 v8, v7
	s_nop 1
	v_permlane16_swap_b32_e32 v8, v7
	v_add_f32_e32 v7, v7, v8
	v_mov_b32_e32 v8, v7
	s_nop 1
	v_permlane32_swap_b32_e32 v8, v7
	v_add_f32_e32 v7, v7, v8
	s_waitcnt lgkmcnt(4)
	v_mul_f32_e32 v9, v97, v225
	v_fmac_f32_e32 v9, v96, v224
	v_mul_f32_e32 v10, v99, v227
	v_fmac_f32_e32 v10, v98, v226
	v_add_f32_e32 v9, v9, v10
	ds_read_b128 v[220:223], v133 offset:37888
	v_add_f32_e32 v9, 0, v9
	s_waitcnt lgkmcnt(5)
	s_nop 0
	s_nop 0
	s_waitcnt lgkmcnt(4)
	v_mul_f32_e32 v11, v93, v229
	v_fmac_f32_e32 v11, v92, v228
	v_mul_f32_e32 v10, v95, v231
	v_fmac_f32_e32 v10, v94, v230
	v_add_f32_e32 v10, v11, v10
	v_add_f32_e32 v9, v9, v10
	ds_read_b128 v[224:227], v133 offset:38912
	s_waitcnt lgkmcnt(5)
	s_nop 0
	s_nop 0
	s_waitcnt lgkmcnt(4)
	v_mul_f32_e32 v11, v89, v209
	v_fmac_f32_e32 v11, v88, v208
	v_mul_f32_e32 v10, v91, v211
	v_fmac_f32_e32 v10, v90, v210
	v_add_f32_e32 v10, v11, v10
	v_add_f32_e32 v9, v9, v10
	ds_read_b128 v[228:231], v133 offset:39936
	s_waitcnt lgkmcnt(5)
	s_nop 0
	s_nop 0
	s_waitcnt lgkmcnt(4)
	v_mul_f32_e32 v11, v85, v213
	v_fmac_f32_e32 v11, v84, v212
	v_mul_f32_e32 v10, v87, v215
	v_fmac_f32_e32 v10, v86, v214
	v_add_f32_e32 v10, v11, v10
	v_add_f32_e32 v9, v9, v10
	ds_read_b128 v[208:211], v133 offset:40960
	s_waitcnt lgkmcnt(5)
	s_nop 0
	s_nop 0
	s_waitcnt lgkmcnt(4)
	v_mul_f32_e32 v11, v81, v217
	v_fmac_f32_e32 v11, v80, v216
	v_mul_f32_e32 v10, v83, v219
	v_fmac_f32_e32 v10, v82, v218
	v_add_f32_e32 v10, v11, v10
	v_add_f32_e32 v9, v9, v10
	ds_read_b128 v[212:215], v133 offset:41984
	s_waitcnt lgkmcnt(5)
	s_nop 0
	s_nop 0
	s_waitcnt lgkmcnt(4)
	v_mul_f32_e32 v11, v77, v221
	v_fmac_f32_e32 v11, v76, v220
	v_mul_f32_e32 v10, v79, v223
	v_fmac_f32_e32 v10, v78, v222
	v_add_f32_e32 v10, v11, v10
	v_add_f32_e32 v9, v9, v10
	ds_read_b128 v[216:219], v133 offset:43008
	s_waitcnt lgkmcnt(4)
	v_mul_f32_e32 v11, v73, v225
	v_fmac_f32_e32 v11, v72, v224
	v_mul_f32_e32 v10, v75, v227
	v_fmac_f32_e32 v10, v74, v226
	v_add_f32_e32 v10, v11, v10
	v_add_f32_e32 v9, v9, v10
	ds_read_b128 v[220:223], v133 offset:44032
	s_waitcnt lgkmcnt(4)
	v_mul_f32_e32 v11, v69, v229
	v_fmac_f32_e32 v11, v68, v228
	v_mul_f32_e32 v10, v71, v231
	v_fmac_f32_e32 v10, v70, v230
	ds_read_b128 v[224:227], v133 offset:45056
	v_add_f32_e32 v10, v11, v10
	v_add_f32_e32 v9, v9, v10
	s_nop 1
	v_add_f32_dpp v9, v9, v9 quad_perm:[1,0,3,2] row_mask:0xf bank_mask:0xf
	s_nop 1
	v_add_f32_dpp v9, v9, v9 quad_perm:[2,3,0,1] row_mask:0xf bank_mask:0xf
	s_nop 1
	v_add_f32_dpp v9, v9, v9 row_half_mirror row_mask:0xf bank_mask:0xf
	s_nop 1
	v_add_f32_dpp v9, v9, v9 row_mirror row_mask:0xf bank_mask:0xf
	v_mov_b32_e32 v10, v9
	s_nop 1
	v_permlane16_swap_b32_e32 v10, v9
	v_add_f32_e32 v9, v9, v10
	v_mov_b32_e32 v10, v9
	s_nop 1
	v_permlane32_swap_b32_e32 v10, v9
	v_add_f32_e32 v9, v9, v10
	s_waitcnt lgkmcnt(4)
	v_mul_f32_e32 v11, v97, v209
	v_fmac_f32_e32 v11, v96, v208
	v_mul_f32_e32 v12, v99, v211
	v_fmac_f32_e32 v12, v98, v210
	v_add_f32_e32 v11, v11, v12
	ds_read_b128 v[228:231], v133 offset:46080
	v_add_f32_e32 v11, 0, v11
	s_waitcnt lgkmcnt(5)
	s_nop 0
	s_nop 0
	s_waitcnt lgkmcnt(4)
	v_mul_f32_e32 v13, v93, v213
	v_fmac_f32_e32 v13, v92, v212
	v_mul_f32_e32 v12, v95, v215
	v_fmac_f32_e32 v12, v94, v214
	v_add_f32_e32 v12, v13, v12
	v_add_f32_e32 v11, v11, v12
	ds_read_b128 v[208:211], v133 offset:47104
	s_waitcnt lgkmcnt(5)
	s_nop 0
	s_nop 0
	s_waitcnt lgkmcnt(4)
	v_mul_f32_e32 v13, v89, v217
	v_fmac_f32_e32 v13, v88, v216
	v_mul_f32_e32 v12, v91, v219
	v_fmac_f32_e32 v12, v90, v218
	v_add_f32_e32 v12, v13, v12
	v_add_f32_e32 v11, v11, v12
	ds_read_b128 v[212:215], v133 offset:48128
	s_waitcnt lgkmcnt(5)
	s_nop 0
	s_nop 0
	s_waitcnt lgkmcnt(4)
	v_mul_f32_e32 v13, v85, v221
	v_fmac_f32_e32 v13, v84, v220
	v_mul_f32_e32 v12, v87, v223
	v_fmac_f32_e32 v12, v86, v222
	v_add_f32_e32 v12, v13, v12
	v_add_f32_e32 v11, v11, v12
	ds_read_b128 v[216:219], v133 offset:49152
	s_waitcnt lgkmcnt(5)
	s_nop 0
	s_nop 0
	s_waitcnt lgkmcnt(4)
	v_mul_f32_e32 v13, v81, v225
	v_fmac_f32_e32 v13, v80, v224
	v_mul_f32_e32 v12, v83, v227
	v_fmac_f32_e32 v12, v82, v226
	v_add_f32_e32 v12, v13, v12
	v_add_f32_e32 v11, v11, v12
	ds_read_b128 v[220:223], v133 offset:50176
	s_waitcnt lgkmcnt(5)
	s_nop 0
	s_nop 0
	s_waitcnt lgkmcnt(4)
	v_mul_f32_e32 v13, v77, v229
	v_fmac_f32_e32 v13, v76, v228
	v_mul_f32_e32 v12, v79, v231
	v_fmac_f32_e32 v12, v78, v230
	v_add_f32_e32 v12, v13, v12
	v_add_f32_e32 v11, v11, v12
	ds_read_b128 v[224:227], v133 offset:51200
	s_waitcnt lgkmcnt(4)
; #define LAS __attribute__((address_space(3)))
; __device__ __forceinline__ void phase_norm_route(const bf16_t* x, const float* g, const float* router, bf16_t* H, int* tok_info, unsigned* cnt, LAS unsigned char* lds, int tid, int wid, int lane) {
;     ...
;             float lg[8];
; #pragma unroll
;             for (int e = 0; e < 8; ++e) { float s = 0.f;
; #pragma unroll
;                 for (int j = 0; j < 8; ++j) { const f32x4 r = *(const LAS f32x4*)(RT + e * 2048 + 4 * lane + 256 * j); s += (v[j][0] * r[0] + v[j][1] * r[1]) + (v[j][2] * r[2] + v[j][3] * r[3]); }
;                 lg[e] = wave_sum(s); }
	v_mul_f32_e32 v13, v73, v209
	v_fmac_f32_e32 v13, v72, v208
	v_mul_f32_e32 v12, v75, v211
	v_fmac_f32_e32 v12, v74, v210
	v_add_f32_e32 v12, v13, v12
	v_add_f32_e32 v11, v11, v12
	ds_read_b128 v[228:231], v133 offset:52224
	s_waitcnt lgkmcnt(4)
	v_mul_f32_e32 v13, v69, v213
	v_fmac_f32_e32 v13, v68, v212
	v_mul_f32_e32 v12, v71, v215
	v_fmac_f32_e32 v12, v70, v214
	ds_read_b128 v[208:211], v133 offset:53248
	v_add_f32_e32 v12, v13, v12
	v_add_f32_e32 v11, v11, v12
	s_nop 1
	v_add_f32_dpp v11, v11, v11 quad_perm:[1,0,3,2] row_mask:0xf bank_mask:0xf
	s_nop 1
	v_add_f32_dpp v11, v11, v11 quad_perm:[2,3,0,1] row_mask:0xf bank_mask:0xf
	s_nop 1
	v_add_f32_dpp v11, v11, v11 row_half_mirror row_mask:0xf bank_mask:0xf
	s_nop 1
	v_add_f32_dpp v11, v11, v11 row_mirror row_mask:0xf bank_mask:0xf
	v_mov_b32_e32 v12, v11
	s_nop 1
	v_permlane16_swap_b32_e32 v12, v11
	v_add_f32_e32 v11, v11, v12
	v_mov_b32_e32 v12, v11
	s_nop 1
	v_permlane32_swap_b32_e32 v12, v11
	v_add_f32_e32 v11, v11, v12
	s_waitcnt lgkmcnt(4)
	v_mul_f32_e32 v13, v97, v217
	v_fmac_f32_e32 v13, v96, v216
	v_mul_f32_e32 v14, v99, v219
	v_fmac_f32_e32 v14, v98, v218
	v_add_f32_e32 v13, v13, v14
	ds_read_b128 v[212:215], v133 offset:54272
	v_add_f32_e32 v13, 0, v13
	s_waitcnt lgkmcnt(5)
	s_nop 0
	s_nop 0
	s_waitcnt lgkmcnt(4)
	v_mul_f32_e32 v15, v93, v221
	v_fmac_f32_e32 v15, v92, v220
	v_mul_f32_e32 v14, v95, v223
	v_fmac_f32_e32 v14, v94, v222
	v_add_f32_e32 v14, v15, v14
	v_add_f32_e32 v13, v13, v14
	ds_read_b128 v[216:219], v133 offset:55296
	s_waitcnt lgkmcnt(5)
	s_nop 0
	s_nop 0
	s_waitcnt lgkmcnt(4)
	v_mul_f32_e32 v15, v89, v225
	v_fmac_f32_e32 v15, v88, v224
	v_mul_f32_e32 v14, v91, v227
	v_fmac_f32_e32 v14, v90, v226
	v_add_f32_e32 v14, v15, v14
	v_add_f32_e32 v13, v13, v14
	ds_read_b128 v[220:223], v133 offset:56320
	s_waitcnt lgkmcnt(5)
	s_nop 0
	s_nop 0
	s_waitcnt lgkmcnt(4)
	v_mul_f32_e32 v15, v85, v229
	v_fmac_f32_e32 v15, v84, v228
	v_mul_f32_e32 v14, v87, v231
	v_fmac_f32_e32 v14, v86, v230
	v_add_f32_e32 v14, v15, v14
	v_add_f32_e32 v13, v13, v14
	ds_read_b128 v[224:227], v133 offset:57344
	s_waitcnt lgkmcnt(5)
	s_nop 0
	s_nop 0
	s_waitcnt lgkmcnt(4)
	v_mul_f32_e32 v15, v81, v209
	v_fmac_f32_e32 v15, v80, v208
	v_mul_f32_e32 v14, v83, v211
	v_fmac_f32_e32 v14, v82, v210
	v_add_f32_e32 v14, v15, v14
	v_add_f32_e32 v13, v13, v14
	ds_read_b128 v[228:231], v133 offset:58368
	s_waitcnt lgkmcnt(5)
	s_nop 0
	s_nop 0
	s_waitcnt lgkmcnt(4)
	v_mul_f32_e32 v15, v77, v213
	v_fmac_f32_e32 v15, v76, v212
	v_mul_f32_e32 v14, v79, v215
	v_fmac_f32_e32 v14, v78, v214
	v_add_f32_e32 v14, v15, v14
	v_add_f32_e32 v13, v13, v14
	ds_read_b128 v[208:211], v133 offset:59392
	s_waitcnt lgkmcnt(4)
	v_mul_f32_e32 v15, v73, v217
	v_fmac_f32_e32 v15, v72, v216
	v_mul_f32_e32 v14, v75, v219
	v_fmac_f32_e32 v14, v74, v218
	v_add_f32_e32 v14, v15, v14
	v_add_f32_e32 v13, v13, v14
	ds_read_b128 v[212:215], v133 offset:60416
	s_waitcnt lgkmcnt(4)
	v_mul_f32_e32 v15, v69, v221
	v_fmac_f32_e32 v15, v68, v220
	v_mul_f32_e32 v14, v71, v223
	v_fmac_f32_e32 v14, v70, v222
	ds_read_b128 v[216:219], v133 offset:61440
	v_add_f32_e32 v14, v15, v14
	v_add_f32_e32 v13, v13, v14
	s_nop 1
	v_add_f32_dpp v13, v13, v13 quad_perm:[1,0,3,2] row_mask:0xf bank_mask:0xf
	s_nop 1
	v_add_f32_dpp v13, v13, v13 quad_perm:[2,3,0,1] row_mask:0xf bank_mask:0xf
	s_nop 1
	v_add_f32_dpp v13, v13, v13 row_half_mirror row_mask:0xf bank_mask:0xf
	s_nop 1
	v_add_f32_dpp v13, v13, v13 row_mirror row_mask:0xf bank_mask:0xf
	v_mov_b32_e32 v14, v13
	s_nop 1
	v_permlane16_swap_b32_e32 v14, v13
	v_add_f32_e32 v13, v13, v14
	v_mov_b32_e32 v14, v13
	s_nop 1
	v_permlane32_swap_b32_e32 v14, v13
	v_add_f32_e32 v13, v13, v14
	s_waitcnt lgkmcnt(4)
	v_mul_f32_e32 v15, v97, v225
	v_fmac_f32_e32 v15, v96, v224
	v_mul_f32_e32 v16, v99, v227
	v_fmac_f32_e32 v16, v98, v226
	v_add_f32_e32 v15, v15, v16
	ds_read_b128 v[220:223], v133 offset:62464
	v_add_f32_e32 v15, 0, v15
	s_waitcnt lgkmcnt(5)
	s_nop 0
	s_nop 0
	s_waitcnt lgkmcnt(4)
	v_mul_f32_e32 v17, v93, v229
	v_fmac_f32_e32 v17, v92, v228
	v_mul_f32_e32 v16, v95, v231
	v_fmac_f32_e32 v16, v94, v230
	v_add_f32_e32 v16, v17, v16
	v_add_f32_e32 v15, v15, v16
	ds_read_b128 v[224:227], v133 offset:63488
	s_waitcnt lgkmcnt(5)
	s_nop 0
	s_nop 0
	s_waitcnt lgkmcnt(4)
	v_mul_f32_e32 v17, v89, v209
	v_fmac_f32_e32 v17, v88, v208
	v_mul_f32_e32 v16, v91, v211
	v_fmac_f32_e32 v16, v90, v210
	v_add_f32_e32 v16, v17, v16
	v_add_f32_e32 v15, v15, v16
	ds_read_b128 v[228:231], v133 offset:64512
	s_waitcnt lgkmcnt(5)
	s_nop 0
	s_nop 0
	s_waitcnt lgkmcnt(4)
	v_mul_f32_e32 v17, v85, v213
	v_fmac_f32_e32 v17, v84, v212
	v_mul_f32_e32 v16, v87, v215
	v_fmac_f32_e32 v16, v86, v214
	v_add_f32_e32 v16, v17, v16
	v_add_f32_e32 v15, v15, v16
	s_waitcnt lgkmcnt(4)
	s_nop 0
	s_nop 0
	s_waitcnt lgkmcnt(3)
	v_mul_f32_e32 v17, v81, v217
	v_fmac_f32_e32 v17, v80, v216
	v_mul_f32_e32 v16, v83, v219
	v_fmac_f32_e32 v16, v82, v218
	v_add_f32_e32 v16, v17, v16
	v_add_f32_e32 v15, v15, v16
	s_waitcnt lgkmcnt(3)
	s_nop 0
	s_nop 0
	s_waitcnt lgkmcnt(2)
	v_mul_f32_e32 v17, v77, v221
	v_fmac_f32_e32 v17, v76, v220
	v_mul_f32_e32 v16, v79, v223
	v_fmac_f32_e32 v16, v78, v222
	v_add_f32_e32 v16, v17, v16
	v_add_f32_e32 v15, v15, v16
	s_waitcnt lgkmcnt(1)
	v_mul_f32_e32 v17, v73, v225
	v_fmac_f32_e32 v17, v72, v224
	v_mul_f32_e32 v16, v75, v227
	v_fmac_f32_e32 v16, v74, v226
	v_add_f32_e32 v16, v17, v16
	v_add_f32_e32 v15, v15, v16
	s_waitcnt lgkmcnt(0)
	v_mul_f32_e32 v17, v69, v229
	v_fmac_f32_e32 v17, v68, v228
	v_mul_f32_e32 v16, v71, v231
	v_fmac_f32_e32 v16, v70, v230
	v_add_f32_e32 v16, v17, v16
	v_add_f32_e32 v15, v15, v16
	s_nop 1
	v_add_f32_dpp v15, v15, v15 quad_perm:[1,0,3,2] row_mask:0xf bank_mask:0xf
	s_nop 1
	v_add_f32_dpp v15, v15, v15 quad_perm:[2,3,0,1] row_mask:0xf bank_mask:0xf
	s_nop 1
	v_add_f32_dpp v15, v15, v15 row_half_mirror row_mask:0xf bank_mask:0xf
	s_nop 1
	v_add_f32_dpp v15, v15, v15 row_mirror row_mask:0xf bank_mask:0xf
	v_mov_b32_e32 v16, v15
	s_nop 1
	v_permlane16_swap_b32_e32 v16, v15
	v_add_f32_e32 v15, v15, v16
	v_mov_b32_e32 v16, v15
	s_nop 1
	v_permlane32_swap_b32_e32 v16, v15
	v_add_f32_e32 v15, v15, v16
	s_waitcnt lgkmcnt(0)
	s_nop 0
	s_nop 0
	s_waitcnt lgkmcnt(0)
	s_nop 0
	s_nop 0
	s_waitcnt lgkmcnt(0)
	s_nop 0
	s_nop 0
	s_waitcnt lgkmcnt(0)
	s_nop 0
	s_nop 0
	s_waitcnt lgkmcnt(0)
	s_nop 0
	s_nop 0
	s_and_saveexec_b64 s[30:31], s[2:3]
	s_cbranch_execz .LBB0_2698
; #define LAS __attribute__((address_space(3)))
; __device__ __forceinline__ void phase_norm_route(const bf16_t* x, const float* g, const float* router, bf16_t* H, int* tok_info, unsigned* cnt, LAS unsigned char* lds, int tid, int wid, int lane) {
;     ...
;             int e1 = 0; float l1 = lg[0];
; #pragma unroll
;             for (int e = 1; e < 8; ++e) if (lg[e] > l1) { l1 = lg[e]; e1 = e; }
;             int e2 = -1; float l2 = -__builtin_inff();
; #pragma unroll
;             for (int e = 0; e < 8; ++e) if (e != e1 && lg[e] > l2) { l2 = lg[e]; e2 = e; }
;             if (lane == 0) {
;                 const float ex = __expf(l2 - l1); const float g1 = 1.0f / (1.0f + ex), g2 = ex / (1.0f + ex);
;                 const int r1 = (int)atomicAdd((unsigned*)(LC + e1), 1u); const int r2 = (int)atomicAdd((unsigned*)(LC + e2), 1u);
;                 LAS int* ti = TI + tl * 8; ti[0] = e1; ti[1] = r1; ti[2] = e2; ti[3] = r2; ti[4] = __float_as_int(g1); ti[5] = __float_as_int(g2);
;             }
	s_nop 0
	s_nop 0
	v_cmp_gt_f32_e32 vcc, v0, v1
	s_nop 0
	s_nop 0
	v_cndmask_b32_e32 v4, v1, v0, vcc
	v_cmp_gt_f32_e64 s[8:9], v2, v4
	s_nop 0
	s_nop 0
	v_cndmask_b32_e64 v4, v4, v2, s[8:9]
	v_cmp_gt_f32_e64 s[10:11], v7, v4
	s_waitcnt lgkmcnt(0)
	s_nop 0
	s_mov_b32 s20, 0xff800000
	v_cndmask_b32_e64 v4, v4, v7, s[10:11]
	v_cmp_gt_f32_e64 s[12:13], v9, v4
	v_cmp_nlg_f32_e64 s[20:21], s20, v1
	s_nop 0
	v_cndmask_b32_e64 v4, v4, v9, s[12:13]
	v_cmp_gt_f32_e64 s[14:15], v11, v4
	s_nop 1
	v_cndmask_b32_e64 v4, v4, v11, s[14:15]
	v_cmp_gt_f32_e64 s[16:17], v13, v4
	s_nop 1
	v_cndmask_b32_e64 v5, v4, v13, s[16:17]
	v_cndmask_b32_e64 v4, 0, 1, vcc
	v_cndmask_b32_e64 v4, v4, 2, s[8:9]
	v_cndmask_b32_e64 v4, v4, 3, s[10:11]
	v_cndmask_b32_e64 v4, v4, 4, s[12:13]
	v_cndmask_b32_e64 v4, v4, 5, s[14:15]
	v_cndmask_b32_e64 v4, v4, 6, s[16:17]
	v_cmp_ngt_f32_e32 vcc, v15, v5
	s_and_b64 s[22:23], s[16:17], vcc
	s_nop 0
	v_cndmask_b32_e32 v4, 7, v4, vcc
	v_cmp_eq_u32_e64 s[18:19], 0, v4
	s_or_b64 s[18:19], s[18:19], s[20:21]
	v_cmp_ne_u32_e64 s[16:17], 1, v4
	v_cndmask_b32_e64 v1, v1, v203, s[18:19]
	v_cmp_gt_f32_e64 s[20:21], v0, v1
	s_and_b64 s[16:17], s[16:17], s[20:21]
	v_cndmask_b32_e64 v0, v1, v0, s[16:17]
	v_cmp_ne_u32_e64 s[14:15], 2, v4
	v_cmp_gt_f32_e64 s[20:21], v2, v0
	s_and_b64 s[14:15], s[14:15], s[20:21]
	v_cndmask_b32_e64 v0, v0, v2, s[14:15]
	v_cmp_ne_u32_e64 s[12:13], 3, v4
	v_cmp_gt_f32_e64 s[20:21], v7, v0
	s_and_b64 s[12:13], s[12:13], s[20:21]
	v_cndmask_b32_e64 v0, v0, v7, s[12:13]
	v_cmp_ne_u32_e64 s[10:11], 4, v4
	v_cmp_gt_f32_e64 s[20:21], v9, v0
	s_and_b64 s[10:11], s[10:11], s[20:21]
	v_cndmask_b32_e64 v0, v0, v9, s[10:11]
	v_cmp_ne_u32_e64 s[8:9], 5, v4
	v_cmp_gt_f32_e64 s[20:21], v11, v0
	s_and_b64 s[8:9], s[8:9], s[20:21]
	v_cndmask_b32_e64 v0, v0, v11, s[8:9]
	v_cmp_ngt_f32_e64 s[20:21], v13, v0
	s_or_b64 s[20:21], s[22:23], s[20:21]
	v_cndmask_b32_e64 v1, 0, -1, s[18:19]
	v_cndmask_b32_e64 v0, v13, v0, s[20:21]
	v_cmp_gt_f32_e64 s[22:23], v15, v0
	s_and_b64 s[22:23], vcc, s[22:23]
	v_cndmask_b32_e64 v1, v1, 1, s[16:17]
	v_cndmask_b32_e64 v0, v0, v15, s[22:23]
	v_cndmask_b32_e32 v2, v15, v5, vcc
	v_cndmask_b32_e64 v1, v1, 2, s[14:15]
	v_sub_f32_e32 v0, v0, v2
	v_cndmask_b32_e64 v1, v1, 3, s[12:13]
	v_mul_f32_e32 v0, 0x3fb8aa3b, v0
	v_cndmask_b32_e64 v1, v1, 4, s[10:11]
	v_exp_f32_e32 v0, v0
	v_cndmask_b32_e64 v1, v1, 5, s[8:9]
	v_cndmask_b32_e64 v1, 6, v1, s[20:21]
	v_cndmask_b32_e64 v6, v1, 7, s[22:23]
	v_lshl_add_u32 v1, v4, 2, s34
	v_add_f32_e32 v2, 1.0, v0
	ds_add_rtn_u32 v5, v1, v188
	v_lshl_add_u32 v1, v6, 2, s34
	ds_add_rtn_u32 v7, v1, v188
	v_div_scale_f32 v1, s[8:9], v2, v2, v0
	v_rcp_f32_e32 v8, v1
	s_add_i32 s10, s35, s38
	s_add_i32 s11, s10, 0x10000
	v_mov_b32_e32 v9, s11
	s_waitcnt lgkmcnt(0)
	ds_write_b128 v9, v[4:7]
	v_fma_f32 v4, -v1, v8, 1.0
	v_fmac_f32_e32 v8, v4, v8
	v_div_scale_f32 v4, vcc, v0, v2, v0
	v_mul_f32_e32 v5, v4, v8
	v_fma_f32 v6, -v1, v5, v4
	v_fmac_f32_e32 v5, v6, v8
	v_fma_f32 v1, -v1, v5, v4
	v_div_scale_f32 v4, s[8:9], v2, v2, 1.0
	v_rcp_f32_e32 v6, v4
	v_div_fmas_f32 v1, v1, v8, v5
	v_div_fixup_f32 v1, v1, v2, v0
	s_add_i32 s10, s10, 0x10010
	v_fma_f32 v0, -v4, v6, 1.0
	v_fmac_f32_e32 v6, v0, v6
	v_div_scale_f32 v0, vcc, 1.0, v2, 1.0
	v_mul_f32_e32 v5, v0, v6
	v_fma_f32 v7, -v4, v5, v0
	v_fmac_f32_e32 v5, v7, v6
	v_fma_f32 v0, -v4, v5, v0
	v_div_fmas_f32 v0, v0, v6, v5
	v_div_fixup_f32 v0, v0, v2, 1.0
	v_mov_b32_e32 v2, s10
	ds_write_b64 v2, v[0:1]
	s_branch .LBB0_2698
